# MLA: counted K-frag waits, hoisted K reads, batched W_uv loads, pipelined epilogue out-proj MFMAs; P11 gfin loads hoisted
# speedup vs baseline: 1.0041x; 1.0041x over previous
.LBB0_1238:
	s_add_i32 s98, s10, -3
	s_and_b32 s98, s98, 2
	s_mulk_i32 s98, 0x6000
	v_add_u32_e32 v144, s98, v147
	ds_read_b128 v[64:67], v144
	ds_read_b128 v[68:71], v144 offset:12288
	v_add_u32_e32 v146, s98, v148
	v_add_u32_e32 v159, s98, v149
	v_add_u32_e32 v168, s98, v150
	ds_read_b128 v[160:163], v146
	ds_read_b128 v[164:167], v146 offset:12288
	ds_read_b128 v[176:179], v159
	ds_read_b128 v[204:207], v159 offset:12288
	ds_read_b128 v[208:211], v168
	ds_read_b128 v[212:215], v168 offset:12288
	s_add_i32 s13, s10, -1
	s_cmp_ge_u32 s13, s9
	s_cbranch_scc1 .LBB0_1240
	s_and_b32 s14, s13, 2
	s_mulk_i32 s14, 0x6000
	s_add_i32 s14, s88, s14
	s_mov_b32 m0, s14
	v_lshl_add_u64 v[224:225], v[174:175], 0, v[180:181]
	global_load_lds_dwordx4 v[174:175], off
	s_add_i32 m0, s14, 0x2000
	v_mov_b32_e32 v185, v181
	global_load_lds_dwordx4 v[172:173], off
	s_add_i32 m0, s14, 0x4000
	s_and_b32 s14, s10, 3
	s_mulk_i32 s14, 0x6000
	s_add_i32 s14, s88, s14
	global_load_lds_dwordx4 v[188:189], off
	s_mov_b32 m0, s14
	v_lshl_add_u64 v[226:227], v[172:173], 0, v[184:185]
	v_mov_b32_e32 v187, v181
	global_load_lds_dwordx4 v[224:225], off
	s_add_i32 m0, s14, 0x2000
	v_lshl_add_u64 v[228:229], v[188:189], 0, v[186:187]
	global_load_lds_dwordx4 v[226:227], off
	s_add_i32 m0, s14, 0x4000
	v_lshl_add_u64 v[174:175], v[224:225], 0, v[180:181]
	global_load_lds_dwordx4 v[228:229], off
	v_lshl_add_u64 v[172:173], v[226:227], 0, v[184:185]
	v_lshl_add_u64 v[188:189], v[228:229], 0, v[186:187]
.LBB0_1240:
	s_add_i32 s14, s10, -3
	s_cmp_gt_u32 s14, 3
	s_cselect_b64 s[16:17], -1, 0
	s_xor_b64 s[18:19], s[62:63], -1
	s_or_b64 s[16:17], s[18:19], s[16:17]
	s_and_b64 vcc, exec, s[16:17]
	s_cbranch_vccnz .LBB0_1242
	s_add_i32 s15, s11, -3
	v_subrev_u32_e32 v224, 24, v155
	v_xor_b32_e32 v226, s15, v183
	v_mad_i64_i32 v[224:225], s[16:17], s20, v224, 0
	v_lshlrev_b32_e32 v226, 4, v226
	v_lshl_add_u64 v[224:225], v[224:225], 2, s[4:5]
	v_and_b32_e32 v226, 0x70, v226
	v_mov_b32_e32 v227, v181
	v_lshl_add_u64 v[224:225], v[224:225], 0, v[226:227]
	s_add_i32 m0, s12, 0xfffff400
	s_add_i32 s15, s11, -2
	global_load_lds_dwordx4 v[224:225], off nt
	v_add_u32_e32 v224, -16, v155
	v_xor_b32_e32 v226, s15, v183
	v_mad_i64_i32 v[224:225], s[16:17], s20, v224, 0
	v_lshlrev_b32_e32 v226, 4, v226
	v_lshl_add_u64 v[224:225], v[224:225], 2, s[4:5]
	v_and_b32_e32 v226, 0x70, v226
	v_lshl_add_u64 v[224:225], v[224:225], 0, v[226:227]
	s_add_i32 m0, s12, 0xfffff800
	s_add_i32 s15, s11, -1
	global_load_lds_dwordx4 v[224:225], off nt
	v_add_u32_e32 v224, -8, v155
	v_xor_b32_e32 v226, s15, v183
	v_mad_i64_i32 v[224:225], s[16:17], s20, v224, 0
	v_lshlrev_b32_e32 v226, 4, v226
	v_lshl_add_u64 v[224:225], v[224:225], 2, s[4:5]
	v_and_b32_e32 v226, 0x70, v226
	v_lshl_add_u64 v[224:225], v[224:225], 0, v[226:227]
	s_add_i32 m0, s12, 0xfffffc00
	v_xor_b32_e32 v226, s11, v183
	global_load_lds_dwordx4 v[224:225], off nt
	v_mad_i64_i32 v[224:225], s[16:17], s20, v155, 0
	v_lshlrev_b32_e32 v226, 4, v226
	v_lshl_add_u64 v[224:225], v[224:225], 2, s[4:5]
	v_and_b32_e32 v226, 0x70, v226
	v_lshl_add_u64 v[224:225], v[224:225], 0, v[226:227]
	s_mov_b32 m0, s12
	s_nop 0
	global_load_lds_dwordx4 v[224:225], off nt
.LBB0_1242:
	s_and_b32 s14, s14, 2
	s_mulk_i32 s14, 0x6000
	s_waitcnt lgkmcnt(7)
	v_mfma_f32_32x32x16_bf16 v[80:95], v[64:67], v[112:115], 0
	s_waitcnt lgkmcnt(6)
	v_mfma_f32_32x32x16_bf16 v[64:79], v[68:71], v[112:115], 0
	s_waitcnt lgkmcnt(5)
	v_mfma_f32_32x32x16_bf16 v[80:95], v[160:163], v[116:119], v[80:95]
	ds_read_b128 v[160:163], v144 offset:128
	ds_read_b128 v[216:219], v144 offset:12416
	s_waitcnt lgkmcnt(6)
	v_mfma_f32_32x32x16_bf16 v[64:79], v[164:167], v[116:119], v[64:79]
	s_waitcnt lgkmcnt(5)
	v_mfma_f32_32x32x16_bf16 v[80:95], v[176:179], v[120:123], v[80:95]
	ds_read_b128 v[164:167], v146 offset:128
	ds_read_b128 v[176:179], v146 offset:12416
	s_waitcnt lgkmcnt(6)
	v_mfma_f32_32x32x16_bf16 v[64:79], v[204:207], v[120:123], v[64:79]
	s_waitcnt lgkmcnt(5)
	v_mfma_f32_32x32x16_bf16 v[80:95], v[208:211], v[124:127], v[80:95]
	ds_read_b128 v[204:207], v159 offset:128
	ds_read_b128 v[208:211], v159 offset:12416
	s_waitcnt lgkmcnt(6)
	v_mfma_f32_32x32x16_bf16 v[64:79], v[212:215], v[124:127], v[64:79]
	s_waitcnt lgkmcnt(5)
	v_mfma_f32_32x32x16_bf16 v[80:95], v[160:163], v[96:99], v[80:95]
	ds_read_b128 v[160:163], v168 offset:128
	ds_read_b128 v[212:215], v168 offset:12416
	s_waitcnt lgkmcnt(6)
	v_mfma_f32_32x32x16_bf16 v[64:79], v[216:219], v[96:99], v[64:79]
	s_waitcnt lgkmcnt(5)
	v_mfma_f32_32x32x16_bf16 v[80:95], v[164:167], v[100:103], v[80:95]
	ds_read_b128 v[164:167], v144 offset:256
	ds_read_b128 v[216:219], v144 offset:12544
	s_waitcnt lgkmcnt(6)
	v_mfma_f32_32x32x16_bf16 v[64:79], v[176:179], v[100:103], v[64:79]
	s_waitcnt lgkmcnt(5)
	v_mfma_f32_32x32x16_bf16 v[80:95], v[204:207], v[104:107], v[80:95]
	ds_read_b128 v[176:179], v146 offset:256
	ds_read_b128 v[204:207], v146 offset:12544
	s_waitcnt lgkmcnt(6)
	v_mfma_f32_32x32x16_bf16 v[64:79], v[208:211], v[104:107], v[64:79]
	s_waitcnt lgkmcnt(5)
	v_mfma_f32_32x32x16_bf16 v[80:95], v[160:163], v[108:111], v[80:95]
	ds_read_b128 v[160:163], v159 offset:256
	ds_read_b128 v[208:211], v159 offset:12544
	s_waitcnt lgkmcnt(6)
	v_mfma_f32_32x32x16_bf16 v[64:79], v[212:215], v[108:111], v[64:79]
	s_waitcnt lgkmcnt(5)
	v_mfma_f32_32x32x16_bf16 v[80:95], v[164:167], v[128:131], v[80:95]
	ds_read_b128 v[164:167], v168 offset:256
	ds_read_b128 v[212:215], v168 offset:12544
	s_waitcnt lgkmcnt(6)
	v_mfma_f32_32x32x16_bf16 v[64:79], v[216:219], v[128:131], v[64:79]
	s_waitcnt lgkmcnt(5)
	v_mfma_f32_32x32x16_bf16 v[80:95], v[176:179], v[132:135], v[80:95]
	s_waitcnt lgkmcnt(4)
	v_mfma_f32_32x32x16_bf16 v[64:79], v[204:207], v[132:135], v[64:79]
	s_waitcnt lgkmcnt(3)
	v_mfma_f32_32x32x16_bf16 v[80:95], v[160:163], v[136:139], v[80:95]
	s_waitcnt lgkmcnt(2)
	v_mfma_f32_32x32x16_bf16 v[64:79], v[208:211], v[136:139], v[64:79]
	s_waitcnt lgkmcnt(1)
	v_mfma_f32_32x32x16_bf16 v[80:95], v[164:167], v[140:143], v[80:95]
	s_waitcnt lgkmcnt(0)
	v_mfma_f32_32x32x16_bf16 v[64:79], v[212:215], v[140:143], v[64:79]
	s_sub_i32 s15, s7, 64
	s_cmp_le_u32 s15, s44
	s_cbranch_scc1 .LBB0_1244
	v_add_u32_e32 v144, 0x7b, v156
	v_cmp_gt_u32_e32 vcc, 2.0, v144
	v_add_u32_e32 v144, 0x5b, v156
	s_nop 4
	v_cndmask_b32_e32 v80, v199, v80, vcc
	v_cmp_gt_u32_e32 vcc, 2.0, v144
	v_add_u32_e32 v144, 0x7a, v156
	s_nop 0
	v_cndmask_b32_e32 v64, v199, v64, vcc
	v_cmp_gt_u32_e32 vcc, 2.0, v144
	v_add_u32_e32 v144, 0x5a, v156
	s_nop 0
	v_cndmask_b32_e32 v81, v199, v81, vcc
	v_cmp_gt_u32_e32 vcc, 2.0, v144
	v_add_u32_e32 v144, 0x79, v156
	s_nop 0
	v_cndmask_b32_e32 v65, v199, v65, vcc
	v_cmp_gt_u32_e32 vcc, 2.0, v144
	v_add_u32_e32 v144, 0x59, v156
	s_nop 0
	v_cndmask_b32_e32 v82, v199, v82, vcc
	v_cmp_gt_u32_e32 vcc, 2.0, v144
	v_add_u32_e32 v144, 0x78, v156
	s_nop 0
	v_cndmask_b32_e32 v66, v199, v66, vcc
	v_cmp_gt_u32_e32 vcc, 2.0, v144
	v_add_u32_e32 v144, 0x58, v156
	s_nop 0
	v_cndmask_b32_e32 v83, v199, v83, vcc
	v_cmp_gt_u32_e32 vcc, 2.0, v144
	v_add_u32_e32 v144, 0x73, v156
	s_nop 0
	v_cndmask_b32_e32 v67, v199, v67, vcc
	v_cmp_gt_u32_e32 vcc, 2.0, v144
	v_add_u32_e32 v144, 0x53, v156
	s_nop 0
	v_cndmask_b32_e32 v84, v199, v84, vcc
	v_cmp_gt_u32_e32 vcc, 2.0, v144
	v_add_u32_e32 v144, 0x72, v156
	s_nop 0
	v_cndmask_b32_e32 v68, v199, v68, vcc
	v_cmp_gt_u32_e32 vcc, 2.0, v144
	v_add_u32_e32 v144, 0x52, v156
	s_nop 0
	v_cndmask_b32_e32 v85, v199, v85, vcc
	v_cmp_gt_u32_e32 vcc, 2.0, v144
	v_add_u32_e32 v144, 0x71, v156
	s_nop 0
	v_cndmask_b32_e32 v69, v199, v69, vcc
	v_cmp_gt_u32_e32 vcc, 2.0, v144
	v_add_u32_e32 v144, 0x51, v156
	s_nop 0
	v_cndmask_b32_e32 v86, v199, v86, vcc
	v_cmp_gt_u32_e32 vcc, 2.0, v144
	v_add_u32_e32 v144, 0x70, v156
	s_nop 0
	v_cndmask_b32_e32 v70, v199, v70, vcc
	v_cmp_gt_u32_e32 vcc, 2.0, v144
	v_add_u32_e32 v144, 0x50, v156
	s_nop 0
	v_cndmask_b32_e32 v87, v199, v87, vcc
	v_cmp_gt_u32_e32 vcc, 2.0, v144
	v_add_u32_e32 v144, 0x6b, v156
	s_nop 0
	v_cndmask_b32_e32 v71, v199, v71, vcc
	v_cmp_gt_u32_e32 vcc, 2.0, v144
	v_add_u32_e32 v144, 0x4b, v156
	s_nop 0
	v_cndmask_b32_e32 v88, v199, v88, vcc
	v_cmp_gt_u32_e32 vcc, 2.0, v144
	v_add_u32_e32 v144, 0x6a, v156
	s_nop 0
	v_cndmask_b32_e32 v72, v199, v72, vcc
	v_cmp_gt_u32_e32 vcc, 2.0, v144
	v_add_u32_e32 v144, 0x4a, v156
	s_nop 0
	v_cndmask_b32_e32 v89, v199, v89, vcc
	v_cmp_gt_u32_e32 vcc, 2.0, v144
	v_add_u32_e32 v144, 0x69, v156
	s_nop 0
	v_cndmask_b32_e32 v73, v199, v73, vcc
	v_cmp_gt_u32_e32 vcc, 2.0, v144
	v_add_u32_e32 v144, 0x49, v156
	s_nop 0
	v_cndmask_b32_e32 v90, v199, v90, vcc
	v_cmp_gt_u32_e32 vcc, 2.0, v144
	v_add_u32_e32 v144, 0x68, v156
	s_nop 0
	v_cndmask_b32_e32 v74, v199, v74, vcc
	v_cmp_gt_u32_e32 vcc, 2.0, v144
	v_add_u32_e32 v144, 0x48, v156
	s_nop 0
	v_cndmask_b32_e32 v91, v199, v91, vcc
	v_cmp_gt_u32_e32 vcc, 2.0, v144
	v_add_u32_e32 v144, 0x63, v156
	s_nop 0
	v_cndmask_b32_e32 v75, v199, v75, vcc
	v_cmp_gt_u32_e32 vcc, 2.0, v144
	v_add_u32_e32 v144, 0x43, v156
	s_nop 0
	v_cndmask_b32_e32 v92, v199, v92, vcc
	v_cmp_gt_u32_e32 vcc, 2.0, v144
	v_add_u32_e32 v144, 0x62, v156
	s_nop 0
	v_cndmask_b32_e32 v76, v199, v76, vcc
	v_cmp_gt_u32_e32 vcc, 2.0, v144
	v_add_u32_e32 v144, 0x42, v156
	s_nop 0
	v_cndmask_b32_e32 v93, v199, v93, vcc
	v_cmp_gt_u32_e32 vcc, 2.0, v144
	v_add_u32_e32 v144, 0x61, v156
	s_nop 0
	v_cndmask_b32_e32 v77, v199, v77, vcc
	v_cmp_gt_u32_e32 vcc, 2.0, v144
	v_add_u32_e32 v144, 0x41, v156
	s_nop 0
	v_cndmask_b32_e32 v94, v199, v94, vcc
	v_cmp_gt_u32_e32 vcc, 2.0, v144
	v_add_u32_e32 v144, 0x60, v156
	s_nop 0
	v_cndmask_b32_e32 v78, v199, v78, vcc
	v_cmp_gt_u32_e32 vcc, 2.0, v144
	v_add_u32_e32 v144, 64, v156
	s_nop 0
	v_cndmask_b32_e32 v95, v199, v95, vcc
	v_cmp_gt_u32_e32 vcc, 2.0, v144
	s_nop 1
	v_cndmask_b32_e32 v79, v199, v79, vcc
.LBB0_1244:
	s_nop 7
	v_max3_f32 v144, v80, v81, v82
	v_max3_f32 v144, v144, v83, v84
	v_max3_f32 v146, v64, v65, v66
	v_max3_f32 v144, v144, v85, v86
	v_max3_f32 v146, v146, v67, v68
	v_max3_f32 v144, v144, v87, v88
	v_max3_f32 v146, v146, v69, v70
	v_max3_f32 v144, v144, v89, v90
	v_max3_f32 v146, v146, v71, v72
	v_max3_f32 v144, v144, v91, v92
	v_max3_f32 v146, v146, v73, v74
	v_max3_f32 v144, v144, v93, v94
	v_max3_f32 v146, v146, v75, v76
	v_max3_f32 v146, v146, v77, v78
	v_max3_f32 v144, v144, v95, v79
	v_max_f32_e32 v144, v144, v146
	v_mov_b32_e32 v146, v144
	s_nop 1
	v_permlane32_swap_b32_e32 v144, v146
	v_max_f32_e32 v146, v146, v146
	v_max_f32_e32 v144, v144, v144
	v_max_f32_e32 v146, v144, v146
	v_sub_f32_e32 v144, v146, v157
	v_cmp_ge_f32_e32 vcc, s0, v144
	s_cmp_eq_u64 vcc, exec
	v_mov_b32_e32 v144, 1.0
	s_cbranch_scc1 .LBB0_1246
	v_max_f32_e32 v144, v146, v146
	v_max_f32_e32 v146, v157, v157
	v_max_f32_e32 v146, v146, v144
	v_sub_f32_e32 v144, v157, v146
	v_exp_f32_e32 v144, v144
	v_mov_b32_e32 v157, v146
	v_pk_mul_f32 v[62:63], v[62:63], v[144:145] op_sel_hi:[1,0]
	v_pk_mul_f32 v[60:61], v[60:61], v[144:145] op_sel_hi:[1,0]
	v_pk_mul_f32 v[58:59], v[58:59], v[144:145] op_sel_hi:[1,0]
	v_pk_mul_f32 v[56:57], v[56:57], v[144:145] op_sel_hi:[1,0]
	v_pk_mul_f32 v[54:55], v[54:55], v[144:145] op_sel_hi:[1,0]
	v_pk_mul_f32 v[52:53], v[52:53], v[144:145] op_sel_hi:[1,0]
	v_pk_mul_f32 v[50:51], v[50:51], v[144:145] op_sel_hi:[1,0]
	v_pk_mul_f32 v[48:49], v[48:49], v[144:145] op_sel_hi:[1,0]
	v_pk_mul_f32 v[46:47], v[46:47], v[144:145] op_sel_hi:[1,0]
	v_pk_mul_f32 v[44:45], v[44:45], v[144:145] op_sel_hi:[1,0]
	v_pk_mul_f32 v[42:43], v[42:43], v[144:145] op_sel_hi:[1,0]
	v_pk_mul_f32 v[40:41], v[40:41], v[144:145] op_sel_hi:[1,0]
	v_pk_mul_f32 v[38:39], v[38:39], v[144:145] op_sel_hi:[1,0]
	v_pk_mul_f32 v[36:37], v[36:37], v[144:145] op_sel_hi:[1,0]
	v_pk_mul_f32 v[34:35], v[34:35], v[144:145] op_sel_hi:[1,0]
	v_pk_mul_f32 v[32:33], v[32:33], v[144:145] op_sel_hi:[1,0]
	v_pk_mul_f32 v[14:15], v[14:15], v[144:145] op_sel_hi:[1,0]
	v_pk_mul_f32 v[12:13], v[12:13], v[144:145] op_sel_hi:[1,0]
	v_pk_mul_f32 v[10:11], v[10:11], v[144:145] op_sel_hi:[1,0]
	v_pk_mul_f32 v[8:9], v[8:9], v[144:145] op_sel_hi:[1,0]
	v_pk_mul_f32 v[6:7], v[6:7], v[144:145] op_sel_hi:[1,0]
	v_pk_mul_f32 v[4:5], v[4:5], v[144:145] op_sel_hi:[1,0]
	v_pk_mul_f32 v[2:3], v[2:3], v[144:145] op_sel_hi:[1,0]
	v_pk_mul_f32 v[0:1], v[0:1], v[144:145] op_sel_hi:[1,0]
	v_pk_mul_f32 v[30:31], v[30:31], v[144:145] op_sel_hi:[1,0]
	v_pk_mul_f32 v[28:29], v[28:29], v[144:145] op_sel_hi:[1,0]
	v_pk_mul_f32 v[26:27], v[26:27], v[144:145] op_sel_hi:[1,0]
	v_pk_mul_f32 v[24:25], v[24:25], v[144:145] op_sel_hi:[1,0]
	v_pk_mul_f32 v[22:23], v[22:23], v[144:145] op_sel_hi:[1,0]
	v_pk_mul_f32 v[20:21], v[20:21], v[144:145] op_sel_hi:[1,0]
	v_pk_mul_f32 v[18:19], v[18:19], v[144:145] op_sel_hi:[1,0]
	v_pk_mul_f32 v[16:17], v[16:17], v[144:145] op_sel_hi:[1,0]
.LBB0_1246:
	v_sub_f32_e32 v80, v80, v157
	v_exp_f32_e32 v80, v80
	v_sub_f32_e32 v81, v81, v157
	v_exp_f32_e32 v81, v81
	v_sub_f32_e32 v82, v82, v157
	v_exp_f32_e32 v82, v82
	v_sub_f32_e32 v83, v83, v157
	v_exp_f32_e32 v83, v83
	v_sub_f32_e32 v84, v84, v157
	v_add_f32_e32 v146, 0, v80
	v_exp_f32_e32 v84, v84
	v_sub_f32_e32 v85, v85, v157
	v_add_f32_e32 v146, v81, v146
	v_exp_f32_e32 v85, v85
	v_sub_f32_e32 v86, v86, v157
	v_add_f32_e32 v146, v82, v146
	v_exp_f32_e32 v86, v86
	v_sub_f32_e32 v87, v87, v157
	v_add_f32_e32 v146, v83, v146
	v_exp_f32_e32 v87, v87
	v_sub_f32_e32 v88, v88, v157
	v_add_f32_e32 v146, v84, v146
	v_exp_f32_e32 v88, v88
	v_sub_f32_e32 v89, v89, v157
	v_add_f32_e32 v146, v85, v146
	v_exp_f32_e32 v89, v89
	v_sub_f32_e32 v90, v90, v157
	v_add_f32_e32 v146, v86, v146
	v_exp_f32_e32 v90, v90
	v_sub_f32_e32 v91, v91, v157
	v_add_f32_e32 v146, v87, v146
	v_exp_f32_e32 v91, v91
	v_sub_f32_e32 v92, v92, v157
	v_add_f32_e32 v146, v88, v146
	v_exp_f32_e32 v92, v92
	v_sub_f32_e32 v93, v93, v157
	v_add_f32_e32 v146, v89, v146
	v_exp_f32_e32 v93, v93
	v_sub_f32_e32 v94, v94, v157
	v_add_f32_e32 v146, v90, v146
	v_exp_f32_e32 v94, v94
	v_sub_f32_e32 v95, v95, v157
	v_add_f32_e32 v146, v91, v146
	v_exp_f32_e32 v95, v95
	v_sub_f32_e32 v64, v64, v157
	v_add_f32_e32 v146, v92, v146
	v_exp_f32_e32 v64, v64
	v_sub_f32_e32 v65, v65, v157
	v_add_f32_e32 v146, v93, v146
	v_exp_f32_e32 v65, v65
	v_sub_f32_e32 v66, v66, v157
	v_add_f32_e32 v146, v94, v146
	v_exp_f32_e32 v66, v66
	v_sub_f32_e32 v67, v67, v157
	v_add_f32_e32 v146, v95, v146
	v_exp_f32_e32 v67, v67
	v_sub_f32_e32 v68, v68, v157
	v_add_f32_e32 v146, v64, v146
	v_exp_f32_e32 v68, v68
	v_sub_f32_e32 v69, v69, v157
	v_add_f32_e32 v146, v65, v146
	v_exp_f32_e32 v69, v69
	v_sub_f32_e32 v70, v70, v157
	v_add_f32_e32 v146, v66, v146
	v_exp_f32_e32 v70, v70
	v_sub_f32_e32 v71, v71, v157
	v_add_f32_e32 v146, v67, v146
	v_exp_f32_e32 v71, v71
	v_sub_f32_e32 v72, v72, v157
	v_add_f32_e32 v146, v68, v146
	v_exp_f32_e32 v161, v72
	v_add_f32_e32 v146, v69, v146
	v_add_f32_e32 v146, v70, v146
	v_add_f32_e32 v146, v71, v146
	v_sub_f32_e32 v73, v73, v157
	v_add_f32_e32 v72, v161, v146
	v_exp_f32_e32 v146, v73
	v_sub_f32_e32 v73, v74, v157
	v_exp_f32_e32 v162, v73
	v_sub_f32_e32 v73, v75, v157
	v_exp_f32_e32 v163, v73
	v_sub_f32_e32 v73, v76, v157
	v_exp_f32_e32 v164, v73
	v_sub_f32_e32 v73, v77, v157
	v_add_f32_e32 v72, v146, v72
	v_exp_f32_e32 v165, v73
	v_sub_f32_e32 v73, v78, v157
	v_add_f32_e32 v72, v162, v72
	v_exp_f32_e32 v166, v73
	v_sub_f32_e32 v73, v79, v157
	v_add_f32_e32 v72, v163, v72
	v_exp_f32_e32 v167, v73
	v_add_f32_e32 v72, v164, v72
	v_add_f32_e32 v72, v165, v72
	v_add_f32_e32 v72, v166, v72
	v_cvt_pk_bf16_f32 v76, v80, v81
	v_cvt_pk_bf16_f32 v77, v84, v85
	v_cvt_pk_bf16_f32 v78, v82, v83
	v_cvt_pk_bf16_f32 v79, v86, v87
	v_cvt_pk_bf16_f32 v64, v64, v65
	v_cvt_pk_bf16_f32 v65, v68, v69
	v_cvt_pk_bf16_f32 v68, v161, v146
	v_add_u32_e32 v146, s14, v151
	v_add_f32_e32 v159, v167, v72
	v_cvt_pk_bf16_f32 v72, v88, v89
	v_cvt_pk_bf16_f32 v73, v92, v93
	v_cvt_pk_bf16_f32 v74, v90, v91
	v_cvt_pk_bf16_f32 v75, v94, v95
	v_add_u32_e32 v161, s14, v152
	ds_read_b64_tr_b16 v[80:81], v146
	ds_read_b64_tr_b16 v[82:83], v161 offset:768
	ds_read_b64_tr_b16 v[84:85], v146 offset:6144
	ds_read_b64_tr_b16 v[86:87], v161 offset:6912
	ds_read_b64_tr_b16 v[88:89], v146 offset:12288
	ds_read_b64_tr_b16 v[90:91], v161 offset:13056
	ds_read_b64_tr_b16 v[92:93], v146 offset:18432
	ds_read_b64_tr_b16 v[94:95], v161 offset:19200
	s_waitcnt lgkmcnt(6)
	v_mfma_f32_32x32x16_bf16 v[48:63], v[80:83], v[76:79], v[48:63]
	v_cvt_pk_bf16_f32 v66, v66, v67
	v_cvt_pk_bf16_f32 v67, v70, v71
	v_cvt_pk_bf16_f32 v71, v166, v167
	v_add_u32_e32 v166, s14, v153
	v_cvt_pk_bf16_f32 v69, v164, v165
	v_cvt_pk_bf16_f32 v70, v162, v163
	v_add_u32_e32 v167, s14, v154
	ds_read_b64_tr_b16 v[162:163], v166
	ds_read_b64_tr_b16 v[164:165], v167 offset:768
	ds_read_b64_tr_b16 v[176:177], v166 offset:6144
	ds_read_b64_tr_b16 v[178:179], v167 offset:6912
	ds_read_b64_tr_b16 v[204:205], v166 offset:12288
	ds_read_b64_tr_b16 v[206:207], v167 offset:13056
	ds_read_b64_tr_b16 v[208:209], v166 offset:18432
	ds_read_b64_tr_b16 v[210:211], v167 offset:19200
	s_waitcnt lgkmcnt(12)
	v_mfma_f32_32x32x16_bf16 v[48:63], v[84:87], v[72:75], v[48:63]
	s_add_i32 s14, s10, -2
	s_and_b32 s14, s14, 3
	s_mulk_i32 s14, 0x6000
	v_mov_b32_e32 v160, v159
	s_nop 1
	v_permlane32_swap_b32_e32 v159, v160
	s_waitcnt lgkmcnt(6)
	v_mfma_f32_32x32x16_bf16 v[32:47], v[162:165], v[76:79], v[32:47]
	v_mfma_f32_32x32x16_bf16 v[48:63], v[88:91], v[64:67], v[48:63]
	s_waitcnt lgkmcnt(4)
	v_mfma_f32_32x32x16_bf16 v[32:47], v[176:179], v[72:75], v[32:47]
	v_mfma_f32_32x32x16_bf16 v[48:63], v[92:95], v[68:71], v[48:63]
	ds_read_b64_tr_b16 v[80:81], v146 offset:128
	ds_read_b64_tr_b16 v[82:83], v161 offset:896
	ds_read_b64_tr_b16 v[92:93], v146 offset:6272
	ds_read_b64_tr_b16 v[94:95], v161 offset:7040
	ds_read_b64_tr_b16 v[212:213], v146 offset:12416
	ds_read_b64_tr_b16 v[214:215], v161 offset:13184
	ds_read_b64_tr_b16 v[88:89], v146 offset:18560
	ds_read_b64_tr_b16 v[90:91], v161 offset:19328
	v_add_u32_e32 v146, s14, v147
	v_add_u32_e32 v161, s14, v148
	s_waitcnt lgkmcnt(10)
	v_mfma_f32_32x32x16_bf16 v[32:47], v[204:207], v[64:67], v[32:47]
	ds_read_b64_tr_b16 v[84:85], v166 offset:128
	ds_read_b64_tr_b16 v[86:87], v167 offset:896
	ds_read_b64_tr_b16 v[162:163], v166 offset:6272
	ds_read_b64_tr_b16 v[164:165], v167 offset:7040
	ds_read_b64_tr_b16 v[176:177], v166 offset:12416
	ds_read_b64_tr_b16 v[178:179], v167 offset:13184
	ds_read_b64_tr_b16 v[204:205], v166 offset:18560
	ds_read_b64_tr_b16 v[206:207], v167 offset:19328
	v_add_u32_e32 v166, s14, v149
	v_add_u32_e32 v167, s14, v150
	s_waitcnt lgkmcnt(14)
	v_mfma_f32_32x32x16_bf16 v[0:15], v[80:83], v[76:79], v[0:15]
	s_waitcnt lgkmcnt(6)
	v_mfma_f32_32x32x16_bf16 v[16:31], v[84:87], v[76:79], v[16:31]
	v_mfma_f32_32x32x16_bf16 v[0:15], v[92:95], v[72:75], v[0:15]
	s_waitcnt lgkmcnt(4)
	v_mfma_f32_32x32x16_bf16 v[16:31], v[162:165], v[72:75], v[16:31]
	v_mfma_f32_32x32x16_bf16 v[0:15], v[212:215], v[64:67], v[0:15]
	s_waitcnt lgkmcnt(2)
	v_mfma_f32_32x32x16_bf16 v[16:31], v[176:179], v[64:67], v[16:31]
	v_mfma_f32_32x32x16_bf16 v[32:47], v[208:211], v[68:71], v[32:47]
	v_mfma_f32_32x32x16_bf16 v[0:15], v[88:91], v[68:71], v[0:15]
	s_waitcnt lgkmcnt(0)
	v_mfma_f32_32x32x16_bf16 v[16:31], v[204:207], v[68:71], v[16:31]
	ds_read_b128 v[64:67], v146
	ds_read_b128 v[68:71], v146 offset:12288
	ds_read_b128 v[162:165], v161
	ds_read_b128 v[176:179], v161 offset:12288
	ds_read_b128 v[204:207], v166
	ds_read_b128 v[208:211], v166 offset:12288
	ds_read_b128 v[212:215], v167
	ds_read_b128 v[216:219], v167 offset:12288
	s_waitcnt lgkmcnt(7)
	v_mfma_f32_32x32x16_bf16 v[80:95], v[64:67], v[112:115], 0
	s_waitcnt lgkmcnt(6)
	v_mfma_f32_32x32x16_bf16 v[64:79], v[68:71], v[112:115], 0
	s_waitcnt lgkmcnt(5)
	v_mfma_f32_32x32x16_bf16 v[80:95], v[162:165], v[116:119], v[80:95]
	ds_read_b128 v[162:165], v146 offset:128
	ds_read_b128 v[220:223], v146 offset:12416
	s_waitcnt lgkmcnt(6)
	v_mfma_f32_32x32x16_bf16 v[64:79], v[176:179], v[116:119], v[64:79]
	s_waitcnt lgkmcnt(5)
	v_mfma_f32_32x32x16_bf16 v[80:95], v[204:207], v[120:123], v[80:95]
	ds_read_b128 v[176:179], v161 offset:128
	ds_read_b128 v[204:207], v161 offset:12416
	s_waitcnt lgkmcnt(6)
	v_mfma_f32_32x32x16_bf16 v[64:79], v[208:211], v[120:123], v[64:79]
	s_waitcnt lgkmcnt(5)
	v_mfma_f32_32x32x16_bf16 v[80:95], v[212:215], v[124:127], v[80:95]
	ds_read_b128 v[208:211], v166 offset:128
	ds_read_b128 v[212:215], v166 offset:12416
	s_waitcnt lgkmcnt(6)
	v_mfma_f32_32x32x16_bf16 v[64:79], v[216:219], v[124:127], v[64:79]
	s_waitcnt lgkmcnt(5)
	v_mfma_f32_32x32x16_bf16 v[80:95], v[162:165], v[96:99], v[80:95]
	ds_read_b128 v[162:165], v167 offset:128
	ds_read_b128 v[216:219], v167 offset:12416
	s_waitcnt lgkmcnt(6)
	v_mfma_f32_32x32x16_bf16 v[64:79], v[220:223], v[96:99], v[64:79]
	s_waitcnt lgkmcnt(5)
	v_mfma_f32_32x32x16_bf16 v[80:95], v[176:179], v[100:103], v[80:95]
	ds_read_b128 v[176:179], v146 offset:256
	ds_read_b128 v[220:223], v146 offset:12544
	s_waitcnt lgkmcnt(6)
	v_mfma_f32_32x32x16_bf16 v[64:79], v[204:207], v[100:103], v[64:79]
	s_waitcnt lgkmcnt(5)
	v_mfma_f32_32x32x16_bf16 v[80:95], v[208:211], v[104:107], v[80:95]
	ds_read_b128 v[204:207], v161 offset:256
	ds_read_b128 v[208:211], v161 offset:12544
	s_waitcnt lgkmcnt(6)
	v_mfma_f32_32x32x16_bf16 v[64:79], v[212:215], v[104:107], v[64:79]
	s_waitcnt lgkmcnt(5)
	v_mfma_f32_32x32x16_bf16 v[80:95], v[162:165], v[108:111], v[80:95]
	ds_read_b128 v[162:165], v166 offset:256
	ds_read_b128 v[212:215], v166 offset:12544
	s_waitcnt lgkmcnt(6)
	v_mfma_f32_32x32x16_bf16 v[64:79], v[216:219], v[108:111], v[64:79]
	s_waitcnt lgkmcnt(5)
	v_mfma_f32_32x32x16_bf16 v[80:95], v[176:179], v[128:131], v[80:95]
	ds_read_b128 v[176:179], v167 offset:256
	ds_read_b128 v[216:219], v167 offset:12544
	s_waitcnt lgkmcnt(6)
	v_mfma_f32_32x32x16_bf16 v[64:79], v[220:223], v[128:131], v[64:79]
	s_waitcnt lgkmcnt(5)
	v_mfma_f32_32x32x16_bf16 v[80:95], v[204:207], v[132:135], v[80:95]
	s_waitcnt lgkmcnt(4)
	v_mfma_f32_32x32x16_bf16 v[64:79], v[208:211], v[132:135], v[64:79]
	s_waitcnt lgkmcnt(3)
	v_mfma_f32_32x32x16_bf16 v[80:95], v[162:165], v[136:139], v[80:95]
	s_waitcnt lgkmcnt(2)
	v_mfma_f32_32x32x16_bf16 v[64:79], v[212:215], v[136:139], v[64:79]
	s_waitcnt lgkmcnt(1)
	v_mfma_f32_32x32x16_bf16 v[80:95], v[176:179], v[140:143], v[80:95]
	s_waitcnt lgkmcnt(0)
	v_mfma_f32_32x32x16_bf16 v[64:79], v[216:219], v[140:143], v[64:79]
	s_cmp_le_u32 s7, s44
	s_cbranch_scc1 .LBB0_1248
	v_add_u32_e32 v146, 59, v156
	v_cmp_gt_u32_e32 vcc, 2.0, v146
	v_add_u32_e32 v146, 27, v156
	s_nop 4
	v_cndmask_b32_e32 v80, v199, v80, vcc
	v_cmp_gt_u32_e32 vcc, 2.0, v146
	v_add_u32_e32 v146, 58, v156
	s_nop 0
	v_cndmask_b32_e32 v64, v199, v64, vcc
	v_cmp_gt_u32_e32 vcc, 2.0, v146
	v_add_u32_e32 v146, 26, v156
	s_nop 0
	v_cndmask_b32_e32 v81, v199, v81, vcc
	v_cmp_gt_u32_e32 vcc, 2.0, v146
	v_add_u32_e32 v146, 57, v156
	s_nop 0
	v_cndmask_b32_e32 v65, v199, v65, vcc
	v_cmp_gt_u32_e32 vcc, 2.0, v146
	v_add_u32_e32 v146, 25, v156
	s_nop 0
	v_cndmask_b32_e32 v82, v199, v82, vcc
	v_cmp_gt_u32_e32 vcc, 2.0, v146
	v_add_u32_e32 v146, 56, v156
	s_nop 0
	v_cndmask_b32_e32 v66, v199, v66, vcc
	v_cmp_gt_u32_e32 vcc, 2.0, v146
	v_add_u32_e32 v146, 24, v156
	s_nop 0
	v_cndmask_b32_e32 v83, v199, v83, vcc
	v_cmp_gt_u32_e32 vcc, 2.0, v146
	v_add_u32_e32 v146, 51, v156
	s_nop 0
	v_cndmask_b32_e32 v67, v199, v67, vcc
	v_cmp_gt_u32_e32 vcc, 2.0, v146
	v_add_u32_e32 v146, 19, v156
	s_nop 0
	v_cndmask_b32_e32 v84, v199, v84, vcc
	v_cmp_gt_u32_e32 vcc, 2.0, v146
	v_add_u32_e32 v146, 50, v156
	s_nop 0
	v_cndmask_b32_e32 v68, v199, v68, vcc
	v_cmp_gt_u32_e32 vcc, 2.0, v146
	v_add_u32_e32 v146, 18, v156
	s_nop 0
	v_cndmask_b32_e32 v85, v199, v85, vcc
	v_cmp_gt_u32_e32 vcc, 2.0, v146
	v_add_u32_e32 v146, 49, v156
	s_nop 0
	v_cndmask_b32_e32 v69, v199, v69, vcc
	v_cmp_gt_u32_e32 vcc, 2.0, v146
	v_add_u32_e32 v146, 17, v156
	s_nop 0
	v_cndmask_b32_e32 v86, v199, v86, vcc
	v_cmp_gt_u32_e32 vcc, 2.0, v146
	v_add_u32_e32 v146, 48, v156
	s_nop 0
	v_cndmask_b32_e32 v70, v199, v70, vcc
	v_cmp_gt_u32_e32 vcc, 2.0, v146
	v_add_u32_e32 v146, 16, v156
	s_nop 0
	v_cndmask_b32_e32 v87, v199, v87, vcc
	v_cmp_gt_u32_e32 vcc, 2.0, v146
	v_add_u32_e32 v146, 43, v156
	s_nop 0
	v_cndmask_b32_e32 v71, v199, v71, vcc
	v_cmp_gt_u32_e32 vcc, 2.0, v146
	v_add_u32_e32 v146, 11, v156
	s_nop 0
	v_cndmask_b32_e32 v88, v199, v88, vcc
	v_cmp_gt_u32_e32 vcc, 2.0, v146
	v_add_u32_e32 v146, 42, v156
	s_nop 0
	v_cndmask_b32_e32 v72, v199, v72, vcc
	v_cmp_gt_u32_e32 vcc, 2.0, v146
	v_add_u32_e32 v146, 10, v156
	s_nop 0
	v_cndmask_b32_e32 v89, v199, v89, vcc
	v_cmp_gt_u32_e32 vcc, 2.0, v146
	v_add_u32_e32 v146, 41, v156
	s_nop 0
	v_cndmask_b32_e32 v73, v199, v73, vcc
	v_cmp_gt_u32_e32 vcc, 2.0, v146
	v_add_u32_e32 v146, 9, v156
	s_nop 0
	v_cndmask_b32_e32 v90, v199, v90, vcc
	v_cmp_gt_u32_e32 vcc, 2.0, v146
	v_add_u32_e32 v146, 40, v156
	s_nop 0
	v_cndmask_b32_e32 v74, v199, v74, vcc
	v_cmp_gt_u32_e32 vcc, 2.0, v146
	v_add_u32_e32 v146, 8, v156
	s_nop 0
	v_cndmask_b32_e32 v91, v199, v91, vcc
	v_cmp_gt_u32_e32 vcc, 2.0, v146
	v_add_u32_e32 v146, 35, v156
	s_nop 0
	v_cndmask_b32_e32 v75, v199, v75, vcc
	v_cmp_gt_u32_e32 vcc, 2.0, v146
	v_add_u32_e32 v146, 3, v156
	s_nop 0
	v_cndmask_b32_e32 v92, v199, v92, vcc
	v_cmp_gt_u32_e32 vcc, 2.0, v146
	v_add_u32_e32 v146, 34, v156
	s_nop 0
	v_cndmask_b32_e32 v76, v199, v76, vcc
	v_cmp_gt_u32_e32 vcc, 2.0, v146
	v_add_u32_e32 v146, 2, v156
	s_nop 0
	v_cndmask_b32_e32 v93, v199, v93, vcc
	v_cmp_gt_u32_e32 vcc, 2.0, v146
	v_add_u32_e32 v146, 33, v156
	s_nop 0
	v_cndmask_b32_e32 v77, v199, v77, vcc
	v_cmp_gt_u32_e32 vcc, 2.0, v146
	v_add_u32_e32 v146, 1, v156
	s_nop 0
	v_cndmask_b32_e32 v94, v199, v94, vcc
	v_cmp_gt_u32_e32 vcc, 2.0, v146
	v_add_u32_e32 v146, 32, v156
	s_nop 0
	v_cndmask_b32_e32 v78, v199, v78, vcc
	v_cmp_gt_u32_e32 vcc, 2.0, v146
	s_nop 1
	v_cndmask_b32_e32 v95, v199, v95, vcc
	v_cmp_gt_u32_e32 vcc, 2.0, v156
	s_nop 1
	v_cndmask_b32_e32 v79, v199, v79, vcc
.LBB0_1248:
	s_nop 7
	v_max3_f32 v146, v80, v81, v82
	v_max3_f32 v146, v146, v83, v84
	v_max3_f32 v161, v64, v65, v66
	v_max3_f32 v146, v146, v85, v86
	v_max3_f32 v161, v161, v67, v68
	v_max3_f32 v146, v146, v87, v88
	v_max3_f32 v161, v161, v69, v70
	v_max3_f32 v146, v146, v89, v90
	v_max3_f32 v161, v161, v71, v72
	v_max3_f32 v146, v146, v91, v92
	v_max3_f32 v161, v161, v73, v74
	v_max3_f32 v146, v146, v93, v94
	v_max3_f32 v161, v161, v75, v76
	v_max3_f32 v161, v161, v77, v78
	v_max3_f32 v146, v146, v95, v79
	v_max_f32_e32 v146, v146, v161
	v_mov_b32_e32 v161, v146
	s_nop 1
	v_permlane32_swap_b32_e32 v146, v161
	v_max_f32_e32 v161, v161, v161
	v_max_f32_e32 v146, v146, v146
	v_max_f32_e32 v161, v146, v161
	v_sub_f32_e32 v146, v161, v157
	v_cmp_ge_f32_e32 vcc, s0, v146
	s_cmp_eq_u64 vcc, exec
	v_mov_b32_e32 v146, 1.0
	s_cbranch_scc1 .LBB0_1237
	v_max_f32_e32 v146, v161, v161
	v_max_f32_e32 v161, v157, v157
	v_max_f32_e32 v161, v161, v146
	v_sub_f32_e32 v146, v157, v161
	v_exp_f32_e32 v146, v146
	v_mov_b32_e32 v157, v161
	v_pk_mul_f32 v[62:63], v[62:63], v[146:147] op_sel_hi:[1,0]
	v_pk_mul_f32 v[60:61], v[60:61], v[146:147] op_sel_hi:[1,0]
	v_pk_mul_f32 v[58:59], v[58:59], v[146:147] op_sel_hi:[1,0]
	v_pk_mul_f32 v[56:57], v[56:57], v[146:147] op_sel_hi:[1,0]
	v_pk_mul_f32 v[54:55], v[54:55], v[146:147] op_sel_hi:[1,0]
	v_pk_mul_f32 v[52:53], v[52:53], v[146:147] op_sel_hi:[1,0]
	v_pk_mul_f32 v[50:51], v[50:51], v[146:147] op_sel_hi:[1,0]
	v_pk_mul_f32 v[48:49], v[48:49], v[146:147] op_sel_hi:[1,0]
	v_pk_mul_f32 v[46:47], v[46:47], v[146:147] op_sel_hi:[1,0]
	v_pk_mul_f32 v[44:45], v[44:45], v[146:147] op_sel_hi:[1,0]
	v_pk_mul_f32 v[42:43], v[42:43], v[146:147] op_sel_hi:[1,0]
	v_pk_mul_f32 v[40:41], v[40:41], v[146:147] op_sel_hi:[1,0]
	v_pk_mul_f32 v[38:39], v[38:39], v[146:147] op_sel_hi:[1,0]
	v_pk_mul_f32 v[36:37], v[36:37], v[146:147] op_sel_hi:[1,0]
	v_pk_mul_f32 v[34:35], v[34:35], v[146:147] op_sel_hi:[1,0]
	v_pk_mul_f32 v[32:33], v[32:33], v[146:147] op_sel_hi:[1,0]
	v_pk_mul_f32 v[14:15], v[14:15], v[146:147] op_sel_hi:[1,0]
	v_pk_mul_f32 v[12:13], v[12:13], v[146:147] op_sel_hi:[1,0]
	v_pk_mul_f32 v[10:11], v[10:11], v[146:147] op_sel_hi:[1,0]
	v_pk_mul_f32 v[8:9], v[8:9], v[146:147] op_sel_hi:[1,0]
	v_pk_mul_f32 v[6:7], v[6:7], v[146:147] op_sel_hi:[1,0]
	v_pk_mul_f32 v[4:5], v[4:5], v[146:147] op_sel_hi:[1,0]
	v_pk_mul_f32 v[2:3], v[2:3], v[146:147] op_sel_hi:[1,0]
	v_pk_mul_f32 v[0:1], v[0:1], v[146:147] op_sel_hi:[1,0]
	v_pk_mul_f32 v[30:31], v[30:31], v[146:147] op_sel_hi:[1,0]
	v_pk_mul_f32 v[28:29], v[28:29], v[146:147] op_sel_hi:[1,0]
	v_pk_mul_f32 v[26:27], v[26:27], v[146:147] op_sel_hi:[1,0]
	v_pk_mul_f32 v[24:25], v[24:25], v[146:147] op_sel_hi:[1,0]
	v_pk_mul_f32 v[22:23], v[22:23], v[146:147] op_sel_hi:[1,0]
	v_pk_mul_f32 v[20:21], v[20:21], v[146:147] op_sel_hi:[1,0]
	v_pk_mul_f32 v[18:19], v[18:19], v[146:147] op_sel_hi:[1,0]
	v_pk_mul_f32 v[16:17], v[16:17], v[146:147] op_sel_hi:[1,0]
	s_branch .LBB0_1237
.LBB0_1250:
	v_ashrrev_i32_e32 v74, 4, v202
	v_lshlrev_b32_e32 v180, 4, v201
	v_ashrrev_i32_e32 v75, 31, v74
	v_lshl_add_u64 v[70:71], s[52:53], 0, v[180:181]
	v_lshlrev_b64 v[64:65], 8, v[74:75]
	v_lshl_add_u64 v[64:65], v[70:71], 0, v[64:65]
	global_load_dwordx4 v[64:67], v[64:65], off
	v_add_u32_e32 v204, 0x200, v202
	v_ashrrev_i32_e32 v76, 4, v204
	v_ashrrev_i32_e32 v77, 31, v76
	v_lshlrev_b64 v[204:205], 8, v[76:77]
	v_lshl_add_u64 v[204:205], v[70:71], 0, v[204:205]
	global_load_dwordx4 v[204:207], v[204:205], off
	v_add_u32_e32 v208, 0x400, v202
	v_ashrrev_i32_e32 v78, 4, v208
	v_ashrrev_i32_e32 v79, 31, v78
	v_lshlrev_b64 v[208:209], 8, v[78:79]
	v_lshl_add_u64 v[208:209], v[70:71], 0, v[208:209]
	global_load_dwordx4 v[208:211], v[208:209], off
	v_add_u32_e32 v212, 0x600, v202
	v_ashrrev_i32_e32 v80, 4, v212
	v_ashrrev_i32_e32 v81, 31, v80
	v_lshlrev_b64 v[212:213], 8, v[80:81]
	v_lshl_add_u64 v[212:213], v[70:71], 0, v[212:213]
	global_load_dwordx4 v[212:215], v[212:213], off
	s_mul_i32 s4, s67, 0xc00
	s_mul_hi_u32 s5, s66, 0xc00
	s_add_i32 s5, s5, s4
	s_mul_i32 s4, s66, 0xc00
	s_add_u32 s20, s80, s4
	v_add_u32_e32 v72, 0, v180
	s_addc_u32 s7, s81, s5
	v_mad_u64_u32 v[74:75], s[4:5], v74, s1, v[72:73]
	v_rcp_f32_e32 v68, v158
	s_and_b32 s21, s7, 0xffff
	s_and_b64 vcc, exec, s[62:63]
	v_readlane_b32 s62, v251, 12
	v_pk_mul_f32 v[48:49], v[68:69], v[48:49] op_sel_hi:[0,1]
	v_pk_mul_f32 v[32:33], v[68:69], v[32:33] op_sel_hi:[0,1]
	v_pk_mul_f32 v[0:1], v[68:69], v[0:1] op_sel_hi:[0,1]
	v_readlane_b32 s63, v251, 13
	s_waitcnt vmcnt(3)
	ds_write_b128 v74, v[64:67]
	v_mad_u64_u32 v[74:75], s[4:5], v76, s1, v[72:73]
	s_waitcnt vmcnt(2)
	ds_write_b128 v74, v[204:207]
	v_mad_u64_u32 v[74:75], s[4:5], v78, s1, v[72:73]
	s_waitcnt vmcnt(1)
	ds_write_b128 v74, v[208:211]
	v_mad_u64_u32 v[70:71], s[4:5], v80, s1, v[72:73]
	s_waitcnt vmcnt(0)
	ds_write_b128 v70, v[212:215]
	v_cvt_pk_bf16_f32 v64, v48, v49
	v_pk_mul_f32 v[48:49], v[68:69], v[50:51] op_sel_hi:[0,1]
	v_cvt_pk_bf16_f32 v65, v48, v49
	v_pk_mul_f32 v[48:49], v[68:69], v[52:53] op_sel_hi:[0,1]
	v_cvt_pk_bf16_f32 v66, v48, v49
	v_pk_mul_f32 v[48:49], v[68:69], v[54:55] op_sel_hi:[0,1]
	v_cvt_pk_bf16_f32 v52, v32, v33
	v_pk_mul_f32 v[32:33], v[68:69], v[34:35] op_sel_hi:[0,1]
	v_cvt_pk_bf16_f32 v67, v48, v49
	v_pk_mul_f32 v[48:49], v[68:69], v[56:57] op_sel_hi:[0,1]
	v_cvt_pk_bf16_f32 v53, v32, v33
	v_pk_mul_f32 v[32:33], v[68:69], v[36:37] op_sel_hi:[0,1]
	v_cvt_pk_bf16_f32 v56, v48, v49
	v_pk_mul_f32 v[48:49], v[68:69], v[58:59] op_sel_hi:[0,1]
	v_cvt_pk_bf16_f32 v54, v32, v33
	v_pk_mul_f32 v[32:33], v[68:69], v[38:39] op_sel_hi:[0,1]
	v_cvt_pk_bf16_f32 v57, v48, v49
	v_pk_mul_f32 v[48:49], v[68:69], v[60:61] op_sel_hi:[0,1]
	v_cvt_pk_bf16_f32 v55, v32, v33
	v_pk_mul_f32 v[32:33], v[68:69], v[40:41] op_sel_hi:[0,1]
	v_cvt_pk_bf16_f32 v40, v0, v1
	v_pk_mul_f32 v[0:1], v[68:69], v[2:3] op_sel_hi:[0,1]
	v_cvt_pk_bf16_f32 v58, v48, v49
	v_pk_mul_f32 v[48:49], v[68:69], v[62:63] op_sel_hi:[0,1]
	v_cvt_pk_bf16_f32 v41, v0, v1
	v_pk_mul_f32 v[0:1], v[68:69], v[4:5] op_sel_hi:[0,1]
	v_cvt_pk_bf16_f32 v59, v48, v49
	v_cvt_pk_bf16_f32 v48, v32, v33
	v_pk_mul_f32 v[32:33], v[68:69], v[42:43] op_sel_hi:[0,1]
	v_cvt_pk_bf16_f32 v42, v0, v1
	v_pk_mul_f32 v[0:1], v[68:69], v[6:7] op_sel_hi:[0,1]
	v_cvt_pk_bf16_f32 v43, v0, v1
	v_pk_mul_f32 v[0:1], v[68:69], v[8:9] op_sel_hi:[0,1]
	v_cvt_pk_bf16_f32 v36, v0, v1
	v_pk_mul_f32 v[0:1], v[68:69], v[10:11] op_sel_hi:[0,1]
	v_cvt_pk_bf16_f32 v37, v0, v1
	v_pk_mul_f32 v[0:1], v[68:69], v[12:13] op_sel_hi:[0,1]
	v_cvt_pk_bf16_f32 v49, v32, v33
	v_pk_mul_f32 v[32:33], v[68:69], v[44:45] op_sel_hi:[0,1]
	v_cvt_pk_bf16_f32 v38, v0, v1
	v_pk_mul_f32 v[0:1], v[68:69], v[14:15] op_sel_hi:[0,1]
	v_cvt_pk_bf16_f32 v50, v32, v33
	v_pk_mul_f32 v[32:33], v[68:69], v[46:47] op_sel_hi:[0,1]
	v_cvt_pk_bf16_f32 v39, v0, v1
	v_pk_mul_f32 v[0:1], v[68:69], v[16:17] op_sel_hi:[0,1]
	v_cvt_pk_bf16_f32 v51, v32, v33
	v_cvt_pk_bf16_f32 v32, v0, v1
	v_pk_mul_f32 v[0:1], v[68:69], v[18:19] op_sel_hi:[0,1]
	v_cvt_pk_bf16_f32 v33, v0, v1
	v_pk_mul_f32 v[0:1], v[68:69], v[20:21] op_sel_hi:[0,1]
	v_cvt_pk_bf16_f32 v34, v0, v1
	v_pk_mul_f32 v[0:1], v[68:69], v[22:23] op_sel_hi:[0,1]
	v_cvt_pk_bf16_f32 v35, v0, v1
	v_pk_mul_f32 v[0:1], v[68:69], v[24:25] op_sel_hi:[0,1]
	v_cvt_pk_bf16_f32 v16, v0, v1
	v_pk_mul_f32 v[0:1], v[68:69], v[26:27] op_sel_hi:[0,1]
	v_cvt_pk_bf16_f32 v17, v0, v1
	v_pk_mul_f32 v[0:1], v[68:69], v[28:29] op_sel_hi:[0,1]
	v_cvt_pk_bf16_f32 v18, v0, v1
	v_pk_mul_f32 v[0:1], v[68:69], v[30:31] op_sel_hi:[0,1]
	v_cvt_pk_bf16_f32 v19, v0, v1
	v_mul_u32_u24_e32 v0, 0x600, v200
	v_or_b32_e32 v20, v145, v0
	v_mul_u32_u24_e32 v0, 0x110, v200
	v_add3_u32 v21, 0, v169, v0
	s_waitcnt lgkmcnt(0)
	s_barrier
	v_lshlrev_b32_e32 v20, 1, v20
	v_add_u32_e32 v26, 0x2000, v21
	v_add_u32_e32 v27, 0x4000, v21
	v_add_u32_e32 v28, 0x6000, v21
	ds_read2_b64 v[76:79], v21 offset1:2
	ds_read2_b64 v[80:83], v21 offset0:4 offset1:6
	ds_read2_b64 v[84:87], v21 offset0:8 offset1:10
	ds_read2_b64 v[88:91], v21 offset0:12 offset1:14
	ds_read2_b64 v[92:95], v21 offset0:16 offset1:18
	ds_read2_b64 v[160:163], v21 offset0:20 offset1:22
	ds_read2_b64 v[164:167], v21 offset0:24 offset1:26
	ds_read2_b64 v[176:179], v21 offset0:28 offset1:30
	ds_read2_b64 v[204:207], v26 offset0:64 offset1:66
	ds_read2_b64 v[208:211], v26 offset0:68 offset1:70
	ds_read2_b64 v[212:215], v26 offset0:72 offset1:74
	ds_read2_b64 v[216:219], v26 offset0:76 offset1:78
	ds_read2_b64 v[220:223], v26 offset0:80 offset1:82
	ds_read2_b64 v[22:25], v26 offset0:84 offset1:86
	ds_read2_b64 v[68:71], v26 offset0:88 offset1:90
	ds_read2_b64 v[72:75], v26 offset0:92 offset1:94
	s_waitcnt lgkmcnt(8)
	v_mfma_f32_32x32x16_bf16 v[0:15], v[76:79], v[64:67], 0
	v_mfma_f32_32x32x16_bf16 v[0:15], v[80:83], v[56:59], v[0:15]
	v_mfma_f32_32x32x16_bf16 v[0:15], v[84:87], v[52:55], v[0:15]
	v_mfma_f32_32x32x16_bf16 v[0:15], v[88:91], v[48:51], v[0:15]
	v_mfma_f32_32x32x16_bf16 v[0:15], v[92:95], v[40:43], v[0:15]
	v_mfma_f32_32x32x16_bf16 v[0:15], v[160:163], v[36:39], v[0:15]
	v_mfma_f32_32x32x16_bf16 v[0:15], v[164:167], v[32:35], v[0:15]
	v_mfma_f32_32x32x16_bf16 v[0:15], v[176:179], v[16:19], v[0:15]
	ds_read2_b64 v[76:79], v27 offset0:128 offset1:130
	ds_read2_b64 v[80:83], v27 offset0:132 offset1:134
	ds_read2_b64 v[84:87], v27 offset0:136 offset1:138
	ds_read2_b64 v[88:91], v27 offset0:140 offset1:142
	ds_read2_b64 v[92:95], v27 offset0:144 offset1:146
	ds_read2_b64 v[160:163], v27 offset0:148 offset1:150
	ds_read2_b64 v[164:167], v27 offset0:152 offset1:154
	ds_read2_b64 v[176:179], v27 offset0:156 offset1:158
	s_nop 11
	v_cvt_pk_bf16_f32 v0, v0, v1
	v_cvt_pk_bf16_f32 v1, v2, v3
	buffer_store_dwordx2 v[0:1], v20, s[20:23], 0 offen sc1
	v_cvt_pk_bf16_f32 v0, v4, v5
	v_cvt_pk_bf16_f32 v1, v6, v7
	buffer_store_dwordx2 v[0:1], v20, s[20:23], 0 offen offset:16 sc1
	v_cvt_pk_bf16_f32 v0, v8, v9
	v_cvt_pk_bf16_f32 v1, v10, v11
	buffer_store_dwordx2 v[0:1], v20, s[20:23], 0 offen offset:32 sc1
	v_cvt_pk_bf16_f32 v0, v12, v13
	v_cvt_pk_bf16_f32 v1, v14, v15
	buffer_store_dwordx2 v[0:1], v20, s[20:23], 0 offen offset:48 sc1
	s_waitcnt lgkmcnt(8)
	v_mfma_f32_32x32x16_bf16 v[0:15], v[204:207], v[64:67], 0
	v_mfma_f32_32x32x16_bf16 v[0:15], v[208:211], v[56:59], v[0:15]
	v_mfma_f32_32x32x16_bf16 v[0:15], v[212:215], v[52:55], v[0:15]
	v_mfma_f32_32x32x16_bf16 v[0:15], v[216:219], v[48:51], v[0:15]
	v_mfma_f32_32x32x16_bf16 v[0:15], v[220:223], v[40:43], v[0:15]
	v_mfma_f32_32x32x16_bf16 v[0:15], v[22:25], v[36:39], v[0:15]
	v_mfma_f32_32x32x16_bf16 v[0:15], v[68:71], v[32:35], v[0:15]
	v_mfma_f32_32x32x16_bf16 v[0:15], v[72:75], v[16:19], v[0:15]
	ds_read2_b64 v[204:207], v28 offset0:192 offset1:194
	ds_read2_b64 v[208:211], v28 offset0:196 offset1:198
	ds_read2_b64 v[212:215], v28 offset0:200 offset1:202
	ds_read2_b64 v[216:219], v28 offset0:204 offset1:206
	ds_read2_b64 v[220:223], v28 offset0:208 offset1:210
	ds_read2_b64 v[22:25], v28 offset0:212 offset1:214
	ds_read2_b64 v[68:71], v28 offset0:216 offset1:218
	ds_read2_b64 v[72:75], v28 offset0:220 offset1:222
	s_nop 11
	v_cvt_pk_bf16_f32 v0, v0, v1
	v_cvt_pk_bf16_f32 v1, v2, v3
	buffer_store_dwordx2 v[0:1], v20, s[20:23], 0 offen offset:64 sc1
	v_cvt_pk_bf16_f32 v0, v4, v5
	v_cvt_pk_bf16_f32 v1, v6, v7
	buffer_store_dwordx2 v[0:1], v20, s[20:23], 0 offen offset:80 sc1
	v_cvt_pk_bf16_f32 v0, v8, v9
	v_cvt_pk_bf16_f32 v1, v10, v11
	buffer_store_dwordx2 v[0:1], v20, s[20:23], 0 offen offset:96 sc1
	v_cvt_pk_bf16_f32 v0, v12, v13
	v_cvt_pk_bf16_f32 v1, v14, v15
	buffer_store_dwordx2 v[0:1], v20, s[20:23], 0 offen offset:112 sc1
	s_waitcnt lgkmcnt(8)
	v_mfma_f32_32x32x16_bf16 v[0:15], v[76:79], v[64:67], 0
	v_mfma_f32_32x32x16_bf16 v[0:15], v[80:83], v[56:59], v[0:15]
	v_mfma_f32_32x32x16_bf16 v[0:15], v[84:87], v[52:55], v[0:15]
	v_mfma_f32_32x32x16_bf16 v[0:15], v[88:91], v[48:51], v[0:15]
	v_mfma_f32_32x32x16_bf16 v[0:15], v[92:95], v[40:43], v[0:15]
	v_mfma_f32_32x32x16_bf16 v[0:15], v[160:163], v[36:39], v[0:15]
	v_mfma_f32_32x32x16_bf16 v[0:15], v[164:167], v[32:35], v[0:15]
	v_mfma_f32_32x32x16_bf16 v[0:15], v[176:179], v[16:19], v[0:15]
	s_nop 11
	v_cvt_pk_bf16_f32 v0, v0, v1
	v_cvt_pk_bf16_f32 v1, v2, v3
	buffer_store_dwordx2 v[0:1], v20, s[20:23], 0 offen offset:128 sc1
	v_cvt_pk_bf16_f32 v0, v4, v5
	v_cvt_pk_bf16_f32 v1, v6, v7
	buffer_store_dwordx2 v[0:1], v20, s[20:23], 0 offen offset:144 sc1
	v_cvt_pk_bf16_f32 v0, v8, v9
	v_cvt_pk_bf16_f32 v1, v10, v11
	buffer_store_dwordx2 v[0:1], v20, s[20:23], 0 offen offset:160 sc1
	v_cvt_pk_bf16_f32 v0, v12, v13
	v_cvt_pk_bf16_f32 v1, v14, v15
	buffer_store_dwordx2 v[0:1], v20, s[20:23], 0 offen offset:176 sc1
	s_waitcnt lgkmcnt(0)
	v_mfma_f32_32x32x16_bf16 v[0:15], v[204:207], v[64:67], 0
	v_mfma_f32_32x32x16_bf16 v[0:15], v[208:211], v[56:59], v[0:15]
	v_mfma_f32_32x32x16_bf16 v[0:15], v[212:215], v[52:55], v[0:15]
	v_mfma_f32_32x32x16_bf16 v[0:15], v[216:219], v[48:51], v[0:15]
	v_mfma_f32_32x32x16_bf16 v[0:15], v[220:223], v[40:43], v[0:15]
	v_mfma_f32_32x32x16_bf16 v[0:15], v[22:25], v[36:39], v[0:15]
	v_mfma_f32_32x32x16_bf16 v[0:15], v[68:71], v[32:35], v[0:15]
	v_mfma_f32_32x32x16_bf16 v[0:15], v[72:75], v[16:19], v[0:15]
	s_nop 11
	v_cvt_pk_bf16_f32 v0, v0, v1
	v_cvt_pk_bf16_f32 v1, v2, v3
	buffer_store_dwordx2 v[0:1], v20, s[20:23], 0 offen offset:192 sc1
	v_cvt_pk_bf16_f32 v0, v4, v5
	v_cvt_pk_bf16_f32 v1, v6, v7
	buffer_store_dwordx2 v[0:1], v20, s[20:23], 0 offen offset:208 sc1
	v_cvt_pk_bf16_f32 v0, v8, v9
	v_cvt_pk_bf16_f32 v1, v10, v11
	buffer_store_dwordx2 v[0:1], v20, s[20:23], 0 offen offset:224 sc1
	v_cvt_pk_bf16_f32 v0, v12, v13
	v_cvt_pk_bf16_f32 v1, v14, v15
	buffer_store_dwordx2 v[0:1], v20, s[20:23], 0 offen offset:240 sc1
	s_cbranch_vccz .LBB0_1339
	s_lshl_b32 s8, s8, 6
	s_ashr_i32 s9, s8, 31
	s_cmp_eq_u64 s[64:65], 0
	s_cbranch_scc1 .LBB0_1253
	s_lshl_b64 s[4:5], s[8:9], 2
	s_add_u32 s4, s64, s4
	s_addc_u32 s5, s65, s5
	v_lshlrev_b32_e32 v4, 2, v182
	global_load_dwordx4 v[0:3], v4, s[4:5] offset:16
	s_nop 0
	global_load_dwordx4 v[4:7], v4, s[4:5]
	s_branch .LBB0_1254

.LBB0_2217:
	v_add_u32_e32 v134, s16, v128
	v_ashrrev_i32_e32 v135, 31, v134
	v_lshlrev_b64 v[144:145], 2, v[134:135]
	v_lshl_add_u64 v[128:129], s[8:9], 0, v[144:145]
	global_load_dwordx4 v[200:203], v[128:129], off
	global_load_dwordx4 v[204:207], v[128:129], off offset:16
	global_load_dwordx4 v[208:211], v[128:129], off offset:512
	global_load_dwordx4 v[212:215], v[128:129], off offset:528
	s_waitcnt vmcnt(0)
	s_waitcnt lgkmcnt(0)
	v_pk_mul_f32 v[118:119], v[118:119], v[142:143] op_sel_hi:[1,0]
	v_pk_mul_f32 v[120:121], v[120:121], v[142:143] op_sel_hi:[1,0]
	v_lshl_add_u64 v[130:131], v[130:131], 2, s[10:11]
	v_pk_mul_f32 v[156:157], v[114:115], v[142:143] op_sel_hi:[1,0]
	v_pk_mul_f32 v[158:159], v[116:117], v[142:143] op_sel_hi:[1,0]
	v_lshl_add_u64 v[144:145], v[130:131], 0, v[144:145]
	v_pk_mul_f32 v[122:123], v[122:123], v[142:143] op_sel_hi:[1,0]
	v_pk_mul_f32 v[124:125], v[124:125], v[142:143] op_sel_hi:[1,0]
	v_pk_mul_f32 v[126:127], v[126:127], v[142:143] op_sel_hi:[1,0]
	s_andn2_b64 vcc, exec, s[2:3]
	v_pk_mul_f32 v[116:117], v[202:203], v[120:121]
	v_pk_mul_f32 v[114:115], v[200:201], v[118:119]
	v_pk_mul_f32 v[120:121], v[206:207], v[158:159]
	v_pk_mul_f32 v[118:119], v[204:205], v[156:157]
	global_store_dwordx4 v[144:145], v[114:117], off
	global_store_dwordx4 v[144:145], v[118:121], off offset:16
	v_pk_mul_f32 v[144:145], v[112:113], v[142:143] op_sel_hi:[1,0]
	v_cndmask_b32_e64 v113, 0, 1, s[2:3]
	v_add_u32_e32 v112, 0x80, v134
	v_cmp_ne_u32_e64 s[0:1], 1, v113
	v_ashrrev_i32_e32 v113, 31, v112
	v_lshl_add_u64 v[130:131], v[112:113], 2, v[130:131]
	v_pk_mul_f32 v[116:117], v[122:123], v[210:211]
	v_pk_mul_f32 v[114:115], v[144:145], v[208:209]
	v_pk_mul_f32 v[120:121], v[126:127], v[214:215]
	v_pk_mul_f32 v[118:119], v[124:125], v[212:213]
	global_store_dwordx4 v[130:131], v[114:117], off
	global_store_dwordx4 v[130:131], v[118:121], off offset:16
	s_cbranch_vccnz .LBB0_2219
	v_lshl_add_u32 v114, v143, 2, 0
	ds_read_b32 v136, v114 offset:4160
.LBB0_2219:
	v_add3_u32 v122, s22, v143, 16
	v_ashrrev_i32_e32 v123, 31, v122
	s_waitcnt lgkmcnt(0)
	v_pk_mul_f32 v[124:125], v[98:99], v[136:137] op_sel_hi:[1,0]
	v_lshlrev_b64 v[98:99], 12, v[122:123]
	v_pk_mul_f32 v[104:105], v[104:105], v[136:137] op_sel_hi:[1,0]
	v_pk_mul_f32 v[106:107], v[106:107], v[136:137] op_sel_hi:[1,0]
	v_lshl_add_u64 v[122:123], s[10:11], 0, v[98:99]
	v_pk_mul_f32 v[126:127], v[100:101], v[136:137] op_sel_hi:[1,0]
	v_lshl_add_u64 v[130:131], v[134:135], 2, v[122:123]
	v_pk_mul_f32 v[102:103], v[102:103], v[136:137] op_sel_hi:[1,0]
	v_pk_mul_f32 v[108:109], v[108:109], v[136:137] op_sel_hi:[1,0]
	v_pk_mul_f32 v[110:111], v[110:111], v[136:137] op_sel_hi:[1,0]
	s_and_b64 vcc, exec, s[0:1]
	v_pk_mul_f32 v[100:101], v[202:203], v[106:107]
	v_pk_mul_f32 v[98:99], v[200:201], v[104:105]
	v_pk_mul_f32 v[106:107], v[206:207], v[126:127]
	v_pk_mul_f32 v[104:105], v[204:205], v[124:125]
	global_store_dwordx4 v[130:131], v[98:101], off
	global_store_dwordx4 v[130:131], v[104:107], off offset:16
	v_pk_mul_f32 v[114:115], v[96:97], v[136:137] op_sel_hi:[1,0]
	v_lshl_add_u64 v[116:117], v[112:113], 2, v[122:123]
	v_mov_b32_e32 v96, 0x7fc00000
	v_pk_mul_f32 v[100:101], v[102:103], v[210:211]
	v_pk_mul_f32 v[98:99], v[114:115], v[208:209]
	v_pk_mul_f32 v[106:107], v[110:111], v[214:215]
	v_pk_mul_f32 v[104:105], v[108:109], v[212:213]
	global_store_dwordx4 v[116:117], v[98:101], off
	global_store_dwordx4 v[116:117], v[104:107], off offset:16
	s_nop 0
	v_mov_b32_e32 v98, 0x7fc00000
	s_cbranch_vccnz .LBB0_2221
	v_lshl_add_u32 v97, v143, 2, 0
	ds_read_b32 v98, v97 offset:4224
.LBB0_2221:
	v_add3_u32 v108, s22, v143, 32
	v_ashrrev_i32_e32 v109, 31, v108
	s_waitcnt lgkmcnt(0)
	v_pk_mul_f32 v[110:111], v[82:83], v[98:99] op_sel_hi:[1,0]
	v_lshlrev_b64 v[82:83], 12, v[108:109]
	v_pk_mul_f32 v[88:89], v[88:89], v[98:99] op_sel_hi:[1,0]
	v_pk_mul_f32 v[90:91], v[90:91], v[98:99] op_sel_hi:[1,0]
	v_lshl_add_u64 v[108:109], s[10:11], 0, v[82:83]
	v_pk_mul_f32 v[114:115], v[84:85], v[98:99] op_sel_hi:[1,0]
	v_lshl_add_u64 v[116:117], v[134:135], 2, v[108:109]
	v_pk_mul_f32 v[80:81], v[80:81], v[98:99] op_sel_hi:[1,0]
	v_pk_mul_f32 v[86:87], v[86:87], v[98:99] op_sel_hi:[1,0]
	v_pk_mul_f32 v[92:93], v[92:93], v[98:99] op_sel_hi:[1,0]
	v_pk_mul_f32 v[94:95], v[94:95], v[98:99] op_sel_hi:[1,0]
	s_and_b64 vcc, exec, s[0:1]
	v_lshl_add_u64 v[98:99], v[112:113], 2, v[108:109]
	v_pk_mul_f32 v[84:85], v[202:203], v[90:91]
	v_pk_mul_f32 v[82:83], v[200:201], v[88:89]
	v_pk_mul_f32 v[90:91], v[206:207], v[114:115]
	v_pk_mul_f32 v[88:89], v[204:205], v[110:111]
	global_store_dwordx4 v[116:117], v[82:85], off
	s_nop 1
	global_store_dwordx4 v[116:117], v[88:91], off offset:16
	v_pk_mul_f32 v[84:85], v[86:87], v[210:211]
	v_pk_mul_f32 v[82:83], v[80:81], v[208:209]
	v_pk_mul_f32 v[90:91], v[94:95], v[214:215]
	v_pk_mul_f32 v[88:89], v[92:93], v[212:213]
	global_store_dwordx4 v[98:99], v[82:85], off
	global_store_dwordx4 v[98:99], v[88:91], off offset:16
	s_cbranch_vccnz .LBB0_2223
	v_lshl_add_u32 v80, v143, 2, 0
	ds_read_b32 v96, v80 offset:4288
.LBB0_2223:
	v_add3_u32 v88, s22, v143, 48
	v_ashrrev_i32_e32 v89, 31, v88
	s_waitcnt lgkmcnt(0)
	v_pk_mul_f32 v[90:91], v[66:67], v[96:97] op_sel_hi:[1,0]
	v_lshlrev_b64 v[66:67], 12, v[88:89]
	v_pk_mul_f32 v[72:73], v[72:73], v[96:97] op_sel_hi:[1,0]
	v_pk_mul_f32 v[74:75], v[74:75], v[96:97] op_sel_hi:[1,0]
	v_lshl_add_u64 v[88:89], s[10:11], 0, v[66:67]
	v_pk_mul_f32 v[92:93], v[68:69], v[96:97] op_sel_hi:[1,0]
	v_lshl_add_u64 v[94:95], v[134:135], 2, v[88:89]
	v_pk_mul_f32 v[70:71], v[70:71], v[96:97] op_sel_hi:[1,0]
	v_pk_mul_f32 v[76:77], v[76:77], v[96:97] op_sel_hi:[1,0]
	v_pk_mul_f32 v[78:79], v[78:79], v[96:97] op_sel_hi:[1,0]
	s_and_b64 vcc, exec, s[0:1]
	v_pk_mul_f32 v[68:69], v[202:203], v[74:75]
	v_pk_mul_f32 v[66:67], v[200:201], v[72:73]
	v_pk_mul_f32 v[74:75], v[206:207], v[92:93]
	v_pk_mul_f32 v[72:73], v[204:205], v[90:91]
	global_store_dwordx4 v[94:95], v[66:69], off
	global_store_dwordx4 v[94:95], v[72:75], off offset:16
	v_pk_mul_f32 v[80:81], v[64:65], v[96:97] op_sel_hi:[1,0]
	v_lshl_add_u64 v[82:83], v[112:113], 2, v[88:89]
	v_mov_b32_e32 v64, 0x7fc00000
	v_pk_mul_f32 v[68:69], v[70:71], v[210:211]
	v_pk_mul_f32 v[66:67], v[80:81], v[208:209]
	v_pk_mul_f32 v[74:75], v[78:79], v[214:215]
	v_pk_mul_f32 v[72:73], v[76:77], v[212:213]
	global_store_dwordx4 v[82:83], v[66:69], off
	global_store_dwordx4 v[82:83], v[72:75], off offset:16
	s_nop 0
	v_mov_b32_e32 v66, 0x7fc00000
	s_cbranch_vccnz .LBB0_2225
	v_lshl_add_u32 v65, v143, 2, 0
	ds_read_b32 v66, v65 offset:4608
.LBB0_2225:
	v_add_u32_e32 v76, s22, v146
	v_ashrrev_i32_e32 v77, 31, v76
	s_waitcnt lgkmcnt(0)
	v_pk_mul_f32 v[78:79], v[50:51], v[66:67] op_sel_hi:[1,0]
	v_lshlrev_b64 v[50:51], 12, v[76:77]
	v_pk_mul_f32 v[56:57], v[56:57], v[66:67] op_sel_hi:[1,0]
	v_pk_mul_f32 v[58:59], v[58:59], v[66:67] op_sel_hi:[1,0]
	v_lshl_add_u64 v[76:77], s[10:11], 0, v[50:51]
	v_pk_mul_f32 v[80:81], v[52:53], v[66:67] op_sel_hi:[1,0]
	v_lshl_add_u64 v[82:83], v[134:135], 2, v[76:77]
	v_pk_mul_f32 v[48:49], v[48:49], v[66:67] op_sel_hi:[1,0]
	v_pk_mul_f32 v[54:55], v[54:55], v[66:67] op_sel_hi:[1,0]
	v_pk_mul_f32 v[60:61], v[60:61], v[66:67] op_sel_hi:[1,0]
	v_pk_mul_f32 v[62:63], v[62:63], v[66:67] op_sel_hi:[1,0]
	s_and_b64 vcc, exec, s[0:1]
	v_lshl_add_u64 v[66:67], v[112:113], 2, v[76:77]
	v_pk_mul_f32 v[52:53], v[202:203], v[58:59]
	v_pk_mul_f32 v[50:51], v[200:201], v[56:57]
	v_pk_mul_f32 v[58:59], v[206:207], v[80:81]
	v_pk_mul_f32 v[56:57], v[204:205], v[78:79]
	global_store_dwordx4 v[82:83], v[50:53], off
	s_nop 1
	global_store_dwordx4 v[82:83], v[56:59], off offset:16
	v_pk_mul_f32 v[52:53], v[54:55], v[210:211]
	v_pk_mul_f32 v[50:51], v[48:49], v[208:209]
	v_pk_mul_f32 v[58:59], v[62:63], v[214:215]
	v_pk_mul_f32 v[56:57], v[60:61], v[212:213]
	global_store_dwordx4 v[66:67], v[50:53], off
	global_store_dwordx4 v[66:67], v[56:59], off offset:16
	s_cbranch_vccnz .LBB0_2227
	v_lshl_add_u32 v48, v143, 2, 0
	ds_read_b32 v64, v48 offset:4672
.LBB0_2227:
	v_lshlrev_b64 v[56:57], 12, v[138:139]
	s_waitcnt lgkmcnt(0)
	v_pk_mul_f32 v[40:41], v[40:41], v[64:65] op_sel_hi:[1,0]
	v_pk_mul_f32 v[42:43], v[42:43], v[64:65] op_sel_hi:[1,0]
	v_lshl_add_u64 v[56:57], s[10:11], 0, v[56:57]
	v_pk_mul_f32 v[58:59], v[34:35], v[64:65] op_sel_hi:[1,0]
	v_pk_mul_f32 v[60:61], v[36:37], v[64:65] op_sel_hi:[1,0]
	v_lshl_add_u64 v[62:63], v[134:135], 2, v[56:57]
	v_pk_mul_f32 v[38:39], v[38:39], v[64:65] op_sel_hi:[1,0]
	v_pk_mul_f32 v[44:45], v[44:45], v[64:65] op_sel_hi:[1,0]
	v_pk_mul_f32 v[46:47], v[46:47], v[64:65] op_sel_hi:[1,0]
	s_and_b64 vcc, exec, s[0:1]
	v_pk_mul_f32 v[36:37], v[202:203], v[42:43]
	v_pk_mul_f32 v[34:35], v[200:201], v[40:41]
	v_pk_mul_f32 v[42:43], v[206:207], v[60:61]
	v_pk_mul_f32 v[40:41], v[204:205], v[58:59]
	global_store_dwordx4 v[62:63], v[34:37], off
	global_store_dwordx4 v[62:63], v[40:43], off offset:16
	v_pk_mul_f32 v[48:49], v[32:33], v[64:65] op_sel_hi:[1,0]
	v_lshl_add_u64 v[50:51], v[112:113], 2, v[56:57]
	v_mov_b32_e32 v32, 0x7fc00000
	v_pk_mul_f32 v[36:37], v[38:39], v[210:211]
	v_pk_mul_f32 v[34:35], v[48:49], v[208:209]
	v_pk_mul_f32 v[42:43], v[46:47], v[214:215]
	v_pk_mul_f32 v[40:41], v[44:45], v[212:213]
	global_store_dwordx4 v[50:51], v[34:37], off
	global_store_dwordx4 v[50:51], v[40:43], off offset:16
	s_nop 0
	v_mov_b32_e32 v34, 0x7fc00000
	s_cbranch_vccnz .LBB0_2229
	v_lshl_add_u32 v33, v143, 2, 0
	ds_read_b32 v34, v33 offset:4736
.LBB0_2229:
	v_lshlrev_b64 v[44:45], 12, v[140:141]
	s_waitcnt lgkmcnt(0)
	v_pk_mul_f32 v[24:25], v[24:25], v[34:35] op_sel_hi:[1,0]
	v_pk_mul_f32 v[26:27], v[26:27], v[34:35] op_sel_hi:[1,0]
	v_lshl_add_u64 v[44:45], s[10:11], 0, v[44:45]
	v_pk_mul_f32 v[46:47], v[18:19], v[34:35] op_sel_hi:[1,0]
	v_pk_mul_f32 v[48:49], v[20:21], v[34:35] op_sel_hi:[1,0]
	v_lshl_add_u64 v[50:51], v[134:135], 2, v[44:45]
	v_pk_mul_f32 v[16:17], v[16:17], v[34:35] op_sel_hi:[1,0]
	v_pk_mul_f32 v[22:23], v[22:23], v[34:35] op_sel_hi:[1,0]
	v_pk_mul_f32 v[28:29], v[28:29], v[34:35] op_sel_hi:[1,0]
	v_pk_mul_f32 v[30:31], v[30:31], v[34:35] op_sel_hi:[1,0]
	s_and_b64 vcc, exec, s[0:1]
	v_lshl_add_u64 v[34:35], v[112:113], 2, v[44:45]
	v_pk_mul_f32 v[20:21], v[202:203], v[26:27]
	v_pk_mul_f32 v[18:19], v[200:201], v[24:25]
	v_pk_mul_f32 v[26:27], v[206:207], v[48:49]
	v_pk_mul_f32 v[24:25], v[204:205], v[46:47]
	global_store_dwordx4 v[50:51], v[18:21], off
	s_nop 1
	global_store_dwordx4 v[50:51], v[24:27], off offset:16
	v_pk_mul_f32 v[20:21], v[22:23], v[210:211]
	v_pk_mul_f32 v[18:19], v[16:17], v[208:209]
	v_pk_mul_f32 v[26:27], v[30:31], v[214:215]
	v_pk_mul_f32 v[24:25], v[28:29], v[212:213]
	global_store_dwordx4 v[34:35], v[18:21], off
	global_store_dwordx4 v[34:35], v[24:27], off offset:16
	s_cbranch_vccnz .LBB0_2231
	v_lshl_add_u32 v16, v143, 2, 0
	ds_read_b32 v32, v16 offset:4800
.LBB0_2231:
	v_lshlrev_b64 v[24:25], 12, v[132:133]
	s_waitcnt lgkmcnt(0)
	v_pk_mul_f32 v[8:9], v[8:9], v[32:33] op_sel_hi:[1,0]
	v_pk_mul_f32 v[10:11], v[10:11], v[32:33] op_sel_hi:[1,0]
	v_lshl_add_u64 v[24:25], s[10:11], 0, v[24:25]
	v_pk_mul_f32 v[26:27], v[2:3], v[32:33] op_sel_hi:[1,0]
	v_pk_mul_f32 v[28:29], v[4:5], v[32:33] op_sel_hi:[1,0]
	v_lshl_add_u64 v[30:31], v[134:135], 2, v[24:25]
	v_pk_mul_f32 v[0:1], v[0:1], v[32:33] op_sel_hi:[1,0]
	v_pk_mul_f32 v[6:7], v[6:7], v[32:33] op_sel_hi:[1,0]
	v_pk_mul_f32 v[12:13], v[12:13], v[32:33] op_sel_hi:[1,0]
	v_pk_mul_f32 v[14:15], v[14:15], v[32:33] op_sel_hi:[1,0]
	v_pk_mul_f32 v[4:5], v[202:203], v[10:11]
	v_pk_mul_f32 v[2:3], v[200:201], v[8:9]
	v_pk_mul_f32 v[10:11], v[206:207], v[28:29]
	v_pk_mul_f32 v[8:9], v[204:205], v[26:27]
	global_store_dwordx4 v[30:31], v[2:5], off
	global_store_dwordx4 v[30:31], v[8:11], off offset:16
	v_lshl_add_u64 v[16:17], v[112:113], 2, v[24:25]
	v_pk_mul_f32 v[4:5], v[6:7], v[210:211]
	v_pk_mul_f32 v[2:3], v[0:1], v[208:209]
	v_pk_mul_f32 v[10:11], v[14:15], v[214:215]
	v_pk_mul_f32 v[8:9], v[12:13], v[212:213]
	global_store_dwordx4 v[16:17], v[2:5], off
	global_store_dwordx4 v[16:17], v[8:11], off offset:16

	.amdhsa_kernel _Z6mk_fwd4Args
		.amdhsa_group_segment_fixed_size 0
		.amdhsa_private_segment_fixed_size 0
		.amdhsa_kernarg_size 448
		.amdhsa_user_sgpr_count 2
		.amdhsa_user_sgpr_dispatch_ptr 0
		.amdhsa_user_sgpr_queue_ptr 0
		.amdhsa_user_sgpr_kernarg_segment_ptr 1
		.amdhsa_user_sgpr_dispatch_id 0
		.amdhsa_user_sgpr_kernarg_preload_length 0
		.amdhsa_user_sgpr_kernarg_preload_offset 0
		.amdhsa_user_sgpr_private_segment_size 0
		.amdhsa_uses_dynamic_stack 0
		.amdhsa_enable_private_segment 0
		.amdhsa_system_sgpr_workgroup_id_x 1
		.amdhsa_system_sgpr_workgroup_id_y 0
		.amdhsa_system_sgpr_workgroup_id_z 0
		.amdhsa_system_sgpr_workgroup_info 0
		.amdhsa_system_vgpr_workitem_id 0
		.amdhsa_next_free_vgpr 252
		.amdhsa_next_free_sgpr 102
		.amdhsa_accum_offset 252
		.amdhsa_reserve_vcc 1
		.amdhsa_float_round_mode_32 0
		.amdhsa_float_round_mode_16_64 0
		.amdhsa_float_denorm_mode_32 3
		.amdhsa_float_denorm_mode_16_64 3
		.amdhsa_dx10_clamp 1
		.amdhsa_ieee_mode 1
		.amdhsa_fp16_overflow 0
		.amdhsa_tg_split 0
		.amdhsa_exception_fp_ieee_invalid_op 0
		.amdhsa_exception_fp_denorm_src 0
		.amdhsa_exception_fp_ieee_div_zero 0
		.amdhsa_exception_fp_ieee_overflow 0
		.amdhsa_exception_fp_ieee_underflow 0
		.amdhsa_exception_fp_ieee_inexact 0
		.amdhsa_exception_int_div_zero 0
	.end_amdhsa_kernel

amdhsa.kernels:
  - .agpr_count:     0
    .args:
      - .offset:         0
        .size:           192
        .value_kind:     by_value
      - .offset:         192
        .size:           4
        .value_kind:     hidden_block_count_x
      - .offset:         196
        .size:           4
        .value_kind:     hidden_block_count_y
      - .offset:         200
        .size:           4
        .value_kind:     hidden_block_count_z
      - .offset:         204
        .size:           2
        .value_kind:     hidden_group_size_x
      - .offset:         206
        .size:           2
        .value_kind:     hidden_group_size_y
      - .offset:         208
        .size:           2
        .value_kind:     hidden_group_size_z
      - .offset:         210
        .size:           2
        .value_kind:     hidden_remainder_x
      - .offset:         212
        .size:           2
        .value_kind:     hidden_remainder_y
      - .offset:         214
        .size:           2
        .value_kind:     hidden_remainder_z
      - .offset:         232
        .size:           8
        .value_kind:     hidden_global_offset_x
      - .offset:         240
        .size:           8
        .value_kind:     hidden_global_offset_y
      - .offset:         248
        .size:           8
        .value_kind:     hidden_global_offset_z
      - .offset:         256
        .size:           2
        .value_kind:     hidden_grid_dims
      - .offset:         312
        .size:           4
        .value_kind:     hidden_dynamic_lds_size
    .group_segment_fixed_size: 0
    .kernarg_segment_align: 8
    .kernarg_segment_size: 448
    .language:       OpenCL C
    .language_version:
      - 2
      - 0
    .max_flat_workgroup_size: 512
    .name:           _Z6mk_fwd4Args
    .private_segment_fixed_size: 0
    .sgpr_count:     108
    .sgpr_spill_count: 261
    .symbol:         _Z6mk_fwd4Args.kd
    .uniform_work_group_size: 1
    .uses_dynamic_stack: false
    .vgpr_count:     252
    .vgpr_spill_count: 0
    .wavefront_size: 64
